# split grid barrier before attention: arrive (flush + signal), run the weight-conversion slice, then wait for the release and acquire (conversion does not depend on the previous phase)
# baseline (speedup 1.0000x reference)
.LBB0_2066:
	s_add_u32 s0, s96, 0x300000
	s_addc_u32 s1, s97, 0
	v_writelane_b32 v255, s0, 7
	s_cmp_lt_i32 s56, 10
	s_nop 0
	v_writelane_b32 v255, s1, 8
	s_cselect_b64 s[0:1], -1, 0
	s_cmp_gt_i32 s57, 9
	s_cselect_b64 s[2:3], -1, 0
	s_and_b64 s[0:1], s[0:1], s[2:3]
	s_andn2_b64 vcc, exec, s[0:1]
	s_mov_b32 s100, 0
	s_cbranch_vccnz .LBB0_2639
	s_waitcnt vmcnt(0)
	v_mov_b32_e32 v1, v0
	s_and_b32 s3, s86, 7
	v_mov_b32_e32 v1, 0x508000
	global_load_dword v218, v1, s[96:97] offset:12 sc1
	s_cmp_gt_u32 s3, 1
	s_cselect_b64 s[0:1], -1, 0
	s_cmpk_lt_i32 s86, 0x600
	s_cselect_b64 s[4:5], -1, 0
	s_and_b64 s[4:5], s[4:5], s[0:1]
	v_cndmask_b32_e64 v2, 0, 1, s[4:5]
	v_cmp_ne_u32_e64 s[0:1], 1, v2
	s_andn2_b64 vcc, exec, s[4:5]
	v_readfirstlane_b32 s2, v0
	s_cbranch_vccnz .LBB0_2069
	s_ashr_i32 s4, s86, 31
	s_lshr_b32 s4, s4, 29
	s_add_i32 s4, s86, s4
	s_and_b32 s5, s4, -8
	s_sub_i32 s5, s86, s5
	s_cmp_lt_i32 s5, 0
	s_movk_i32 s6, 0xc1
	s_cselect_b32 s6, s6, 0xc0
	s_mul_i32 s5, s5, s6
	s_ashr_i32 s4, s4, 3
	s_add_i32 s5, s5, s4
	s_mul_hi_i32 s4, s5, 0x2aaaaaab
	s_lshr_b32 s6, s4, 31
	s_ashr_i32 s4, s4, 4
	s_add_i32 s4, s4, s6
	s_lshl_b32 s6, s4, 2
	s_mulk_i32 s4, 0x60
	s_sub_i32 s4, s5, s4
	s_bfe_i32 s5, s4, 0x80000
	s_bfe_u32 s5, s5, 0x2000d
	s_add_i32 s5, s4, s5
	s_and_b32 s7, s5, 0xfc
	s_sub_i32 s4, s4, s7
	s_sext_i32_i8 s4, s4
	s_add_i32 s30, s6, s4
	s_bfe_i32 s4, s5, 0x80000
	s_sext_i32_i16 s4, s4
	s_ashr_i32 s28, s4, 2

.LBB0_2589:
	s_waitcnt vmcnt(0)
	v_readlane_b32 s56, v254, 51
	v_readlane_b32 s60, v254, 55
	v_readlane_b32 s57, v254, 52
	v_readlane_b32 s61, v254, 56
	v_readlane_b32 s64, v254, 59
	v_readlane_b32 s65, v254, 60
	v_readlane_b32 s66, v254, 61
	v_readlane_b32 s67, v254, 62
	s_barrier
	v_readlane_b32 s58, v254, 53
	v_readlane_b32 s59, v254, 54
	v_readlane_b32 s62, v254, 57
	v_readlane_b32 s63, v254, 58
	s_mov_b32 s100, 0
	s_cmp_lt_i32 s57, 11
	v_lshrrev_b32_e32 v226, 1, v0
	s_cbranch_scc1 .LBB0_2639

.Lxb9_poll:
	s_waitcnt lgkmcnt(0)
	v_add_u32_e32 v6, 1, v2
	v_mul_lo_u32 v6, v6, v1
	s_nop 1
	v_readfirstlane_b32 s100, v6
	s_branch .LBB0_2638
.Lxb9_lead:
	buffer_wbl2 sc1
	v_readlane_b32 s8, v254, 40
	v_readlane_b32 s9, v254, 41
	v_mov_b32_e32 v4, 0x2400
	v_mov_b32_e32 v5, 1
	s_nop 3
	s_waitcnt vmcnt(0)
	global_atomic_add v4, v5, s[8:9]
	global_atomic_add v4, v5, s[8:9] offset:256
	global_atomic_add v4, v5, s[8:9] offset:512
	global_atomic_add v4, v5, s[8:9] offset:768
	global_atomic_add v4, v5, s[8:9] offset:1024
	global_atomic_add v4, v5, s[8:9] offset:1280
	global_atomic_add v4, v5, s[8:9] offset:1536
	global_atomic_add v4, v5, s[8:9] offset:1792
	global_atomic_add v4, v5, s[8:9] offset:2048
	global_atomic_add v4, v5, s[8:9] offset:2304
	global_atomic_add v4, v5, s[8:9] offset:2560
	global_atomic_add v4, v5, s[8:9] offset:2816
	global_atomic_add v4, v5, s[8:9] offset:3072
	global_atomic_add v4, v5, s[8:9] offset:3328
	global_atomic_add v4, v5, s[8:9] offset:3584
	global_atomic_add v4, v5, s[8:9] offset:3840
	s_branch .Lxb9_poll
.LBB0_2638:
	s_or_b64 exec, exec, s[0:1]
	s_waitcnt lgkmcnt(0)
	s_barrier

.LBB0_3207:
	v_cmp_eq_u32_e32 vcc, 0, v0
	s_and_saveexec_b64 s[2:3], vcc
	s_cbranch_execz .Ldwa_end
	s_cmp_eq_u32 s100, 0
	s_cbranch_scc1 .Ldwa_end
	v_readlane_b32 s98, v254, 43
	s_lshl_b32 s98, s98, 8
	v_readlane_b32 s0, v254, 40
	v_readlane_b32 s1, v254, 41
	s_add_u32 s98, s0, s98
	s_addc_u32 s99, s1, 0
	s_mov_b32 s101, 0
	v_mov_b32_e32 v16, 0x2000
.Ldwa_spin:
	global_load_dword v17, v16, s[98:99] offset:1024 sc1
	s_waitcnt vmcnt(0)
	v_cmp_le_u32_e32 vcc, s100, v17
	s_cbranch_vccnz .Ldwa_acq
	s_sleep 1
	s_add_u32 s101, s101, 1
	s_cmp_lt_u32 s101, 0x10000
	s_cbranch_scc1 .Ldwa_spin
.Ldwa_acq:
	buffer_inv sc1
	s_waitcnt vmcnt(0)
	s_mov_b32 s100, 0
.Ldwa_end:
	s_or_b64 exec, exec, s[2:3]
	s_lshl_b64 s[0:1], s[94:95], 20
	v_readlane_b32 s4, v254, 7
	s_add_u32 s0, s0, s4
	v_readlane_b32 s2, v255, 16
	s_addc_u32 s1, s1, s2
	s_waitcnt vmcnt(30)
	v_mov_b64_e32 v[2:3], 0x200
	v_cmp_lt_i64_e32 vcc, s[0:1], v[2:3]
	s_and_b64 s[2:3], vcc, exec
	s_cselect_b32 s93, s0, 0x200
	v_readlane_b32 s0, v255, 15
	s_add_i32 s74, s4, s0
	v_mov_b32_e32 v1, v0
	s_cmp_ge_i32 s74, s93
	s_waitcnt lgkmcnt(0)
	s_barrier
	s_cbranch_scc1 .LBB0_3458
	s_ashr_i32 s2, s74, 6
	s_ashr_i32 s3, s2, 31
	s_lshl_b32 s1, s74, 8
	s_lshl_b64 s[4:5], s[2:3], 11
	s_and_b32 s24, s1, 0x300
	s_or_b32 s4, s4, s24
	s_mul_i32 s1, s5, 0x3000
	s_mul_hi_u32 s3, s4, 0x3000
	s_ashr_i32 s0, s74, 2
	s_add_i32 s3, s3, s1
	s_mul_i32 s1, s4, 0x3000
	v_readlane_b32 s8, v255, 11
	s_add_u32 s1, s8, s1
	v_readlane_b32 s9, v255, 12
	s_addc_u32 s3, s9, s3
	s_lshl_b32 s6, s0, 7
	s_and_b32 s6, s6, 0x780
	s_lshl_b32 s7, s6, 1
	s_add_u32 s10, s1, s7
	s_addc_u32 s11, s3, 0
	s_mul_hi_i32 s1, s2, 0x1800000
	s_mul_i32 s2, s2, 0x1800000
	s_add_u32 s2, s8, s2
	s_addc_u32 s1, s9, s1
	s_add_u32 s2, s2, s7
	s_addc_u32 s1, s1, 0
	s_add_u32 s70, s2, 0x1000
	s_addc_u32 s71, s1, 0
	s_add_u32 s72, s2, 0x2000
	s_addc_u32 s73, s1, 0
	s_lshl_b64 s[2:3], s[4:5], 11
	v_readlane_b32 s1, v255, 13
	s_add_u32 s1, s1, s2
	v_readlane_b32 s2, v255, 14
	s_addc_u32 s2, s2, s3
	s_add_u32 s76, s1, s6
	s_addc_u32 s77, s2, 0
	s_ashr_i32 s1, s0, 31
	s_lshl_b64 s[0:1], s[0:1], 12
	v_readlane_b32 s2, v255, 7
	v_readlane_b32 s3, v255, 8
	s_add_u32 s8, s2, s0
	v_readfirstlane_b32 s0, v0
	s_addc_u32 s9, s3, s1
	s_lshr_b32 s2, s0, 6
	s_movk_i32 s75, 0x3000
	v_lshl_or_b32 v1, s2, 5, v182
	v_writelane_b32 v255, s10, 27
	s_waitcnt vmcnt(13)
	v_and_b32_e32 v20, 0x78, v199
	s_waitcnt vmcnt(11)
	v_lshlrev_b32_e32 v22, 1, v20
	v_mov_b64_e32 v[2:3], s[10:11]
	v_mad_u64_u32 v[4:5], s[0:1], v1, s75, v[2:3]
	v_or_b32_e32 v1, s24, v227
	v_and_b32_e32 v2, 16, v226
	v_mov_b32_e32 v3, 0
	v_mul_u32_u24_e32 v1, 0x1800, v1
	v_lshl_add_u64 v[4:5], v[4:5], 0, v[2:3]
	v_lshlrev_b32_e32 v2, 1, v1
	v_or_b32_e32 v1, 32, v227
	v_or_b32_e32 v6, s24, v1
	v_mul_u32_u24_e32 v6, 0x1800, v6
	s_waitcnt vmcnt(10)
	v_mov_b32_e32 v23, v3
	v_lshlrev_b32_e32 v6, 1, v6
	v_mov_b32_e32 v7, v3
	v_lshl_add_u64 v[8:9], s[70:71], 0, v[2:3]
	v_lshl_add_u64 v[8:9], v[8:9], 0, v[22:23]
	v_lshl_add_u64 v[10:11], s[70:71], 0, v[6:7]
	v_lshl_add_u64 v[10:11], v[10:11], 0, v[22:23]
	global_load_dwordx4 v[12:15], v[8:9], off
	global_load_dwordx4 v[16:19], v[10:11], off
	s_lshl_b32 s0, s2, 13
	s_add_i32 s0, s0, 0
	s_add_i32 m0, s0, 0x10840
	v_lshl_add_u64 v[8:9], v[4:5], 0, 32
	global_load_lds_dwordx4 v[4:5], off
	s_add_i32 m0, s0, 0x10c40
	s_mov_b64 s[2:3], 0x60
	global_load_lds_dwordx4 v[8:9], off
	v_lshl_add_u64 v[8:9], v[4:5], 0, 64
	s_add_i32 m0, s0, 0x11040
	v_lshl_add_u64 v[6:7], s[72:73], 0, v[6:7]
	global_load_lds_dwordx4 v[8:9], off
	v_lshl_add_u64 v[8:9], v[4:5], 0, s[2:3]
	s_add_i32 m0, s0, 0x11440
	s_mov_b64 s[2:3], 0x80
	global_load_lds_dwordx4 v[8:9], off
	v_lshl_add_u64 v[8:9], v[4:5], 0, s[2:3]
	s_add_i32 m0, s0, 0x11840
	s_mov_b64 s[2:3], 0xa0
	global_load_lds_dwordx4 v[8:9], off
	v_lshl_add_u64 v[8:9], v[4:5], 0, s[2:3]
	s_add_i32 m0, s0, 0x11c40
	s_mov_b64 s[2:3], 0xc0
	global_load_lds_dwordx4 v[8:9], off
	v_lshl_add_u64 v[8:9], v[4:5], 0, s[2:3]
	s_add_i32 m0, s0, 0x12040
	s_mov_b64 s[2:3], 0xe0
	global_load_lds_dwordx4 v[8:9], off
	v_lshl_add_u64 v[4:5], v[4:5], 0, s[2:3]
	s_add_i32 m0, s0, 0x12440
	v_lshl_add_u64 v[8:9], v[6:7], 0, v[22:23]
	global_load_lds_dwordx4 v[4:5], off
	v_lshl_add_u64 v[4:5], s[72:73], 0, v[2:3]
	v_lshl_add_u64 v[4:5], v[4:5], 0, v[22:23]
	global_load_dwordx4 v[4:7], v[4:5], off
	s_nop 0
	global_load_dwordx4 v[8:11], v[8:9], off
	s_movk_i32 s0, 0x70
	v_lshlrev_b32_e32 v2, 8, v227
	v_bitop3_b32 v23, v22, v0, s0 bitop3:0x78
	v_add3_u32 v23, 0, v2, v23
	s_waitcnt vmcnt(0)
	s_waitcnt vmcnt(0)
	ds_write_b128 v23, v[12:15] offset:32768
	ds_write_b128 v23, v[16:19] offset:40960
	v_lshrrev_b32_e32 v12, 3, v0
	v_and_b32_e32 v12, 8, v12
	v_and_or_b32 v13, v227, 16, v12
	v_and_or_b32 v12, v1, 48, v12
	v_lshrrev_b32_e32 v13, 1, v13
	v_bfe_u32 v14, v199, 5, 2
	v_lshrrev_b32_e32 v15, 5, v0
	v_lshrrev_b32_e32 v12, 1, v12
	v_or_b32_e32 v13, v13, v14
	v_and_or_b32 v15, v15, 4, v223
	v_or_b32_e32 v12, v12, v14
	v_writelane_b32 v255, s11, 28
	v_lshlrev_b32_e32 v13, 9, v13
	v_lshlrev_b32_e32 v15, 6, v15
	v_and_b32_e32 v16, 48, v22
	v_lshlrev_b32_e32 v12, 9, v12
	v_lshlrev_b32_e32 v201, 4, v196
	v_cmp_eq_u32_e64 s[2:3], 0, v196
	v_or3_b32 v13, v13, v15, v16
	v_or3_b32 v12, v12, v15, v16
	v_and_b32_e32 v14, 0xc0, v201
	v_and_b32_e32 v15, 32, v225
	v_and_b32_e32 v16, 0x118, v199
	v_writelane_b32 v255, s2, 23
	v_or3_b32 v14, v16, v15, v14
	v_bitop3_b32 v16, v198, v249, s0 bitop3:0x78
	v_writelane_b32 v255, s3, 24
	s_add_i32 s0, 0, 0x10810
	v_writelane_b32 v255, s0, 17
	v_writelane_b32 v255, s8, 25
	v_and_b32_e32 v21, 0x70, v0
	s_movk_i32 s1, 0x60
	v_writelane_b32 v255, s9, 26
	v_add_u32_e32 v203, 0, v14
	v_and_b32_e32 v14, 0x70, v249
	v_writelane_b32 v255, s76, 18
	v_writelane_b32 v254, s70, 24
	v_bitop3_b32 v2, v22, v2, v21 bitop3:0xde
	v_lshl_add_u32 v15, v182, 8, 0
	v_bitop3_b32 v17, v198, v14, 32 bitop3:0x36
	v_bitop3_b32 v19, v198, v14, 64 bitop3:0x36
	v_bitop3_b32 v14, v198, v14, s1 bitop3:0x36
	v_writelane_b32 v255, s77, 19
	v_writelane_b32 v254, s71, 25
	s_mov_b32 s89, 0
	v_sub_u32_e32 v200, v182, v185
	v_or_b32_e32 v199, 64, v227
	v_or_b32_e32 v202, 0x60, v227
	v_cmp_gt_u32_e64 s[4:5], 32, v196
	v_cmp_eq_u32_e64 s[6:7], 0, v197
	v_mov_b32_e32 v183, v3
	v_mov_b32_e32 v187, v3
	s_mov_b32 s91, 0x41000000
	v_lshlrev_b32_e32 v188, 1, v20
	s_mov_b32 s90, 0x3e0293ee
	v_lshlrev_b32_e32 v190, 1, v184
	s_mov_b32 s1, 0xc3e00000
	v_add_u32_e32 v196, 0, v13
	v_add_u32_e32 v197, 0, v12
	v_mov_b32_e32 v18, 0xff800000
	v_add_u32_e32 v198, v15, v16
	v_add_u32_e32 v204, v15, v17
	v_add_u32_e32 v205, v15, v19
	v_add_u32_e32 v206, v15, v14
	v_add_u32_e32 v207, 0, v2
	v_mov_b32_e32 v208, 0xf149f2ca
	v_mov_b32_e32 v209, 0x43e00000
	s_mov_b32 s0, 0
	s_mov_b32 s33, s24
	s_mov_b64 s[86:87], s[72:73]
	v_writelane_b32 v254, s94, 63
	s_waitcnt lgkmcnt(0)
	s_barrier
	v_writelane_b32 v255, s95, 0
	s_branch .LBB0_3210
